# 64-byte alignment of the 8 GEMM K-loop headers and 2 scan recurrence loop headers on top of v105
# speedup vs baseline: 1.0028x; 1.0023x over previous
.LBB0_186:
	s_ashr_i32 s25, s24, 31
	s_lshl_b64 s[28:29], s[24:25], 20
	s_ashr_i32 s27, s26, 31
	v_lshl_add_u64 v[146:147], v[160:161], 0, s[28:29]
	s_lshl_b64 s[28:29], s[26:27], 20
	v_lshl_add_u64 v[150:151], v[128:129], 0, s[28:29]
	v_cndmask_b32_e64 v154, v0, v150, s[4:5]
	v_lshl_add_u64 v[158:159], v[0:1], 0, s[18:19]
	v_mov_b32_e32 v0, 0
	v_cndmask_b32_e64 v153, v3, v147, s[4:5]
	v_cndmask_b32_e64 v152, v2, v146, s[4:5]
	v_cndmask_b32_e64 v155, v1, v151, s[4:5]
	v_lshl_add_u64 v[156:157], v[2:3], 0, s[14:15]
	s_mov_b32 s25, -2
	v_mov_b32_e32 v1, v0
	v_mov_b32_e32 v2, v0
	v_mov_b32_e32 v3, v0
	v_mov_b32_e32 v4, v0
	v_mov_b32_e32 v5, v0
	v_mov_b32_e32 v6, v0
	v_mov_b32_e32 v7, v0
	v_mov_b32_e32 v8, v0
	v_mov_b32_e32 v9, v0
	v_mov_b32_e32 v10, v0
	v_mov_b32_e32 v11, v0
	v_mov_b32_e32 v12, v0
	v_mov_b32_e32 v13, v0
	v_mov_b32_e32 v14, v0
	v_mov_b32_e32 v15, v0
	v_mov_b32_e32 v24, v0
	v_mov_b32_e32 v25, v0
	v_mov_b32_e32 v26, v0
	v_mov_b32_e32 v27, v0
	v_mov_b32_e32 v28, v0
	v_mov_b32_e32 v29, v0
	v_mov_b32_e32 v30, v0
	v_mov_b32_e32 v31, v0
	v_mov_b32_e32 v40, v0
	v_mov_b32_e32 v41, v0
	v_mov_b32_e32 v42, v0
	v_mov_b32_e32 v43, v0
	v_mov_b32_e32 v44, v0
	v_mov_b32_e32 v45, v0
	v_mov_b32_e32 v46, v0
	v_mov_b32_e32 v47, v0
	v_mov_b32_e32 v16, v0
	v_mov_b32_e32 v17, v0
	v_mov_b32_e32 v18, v0
	v_mov_b32_e32 v19, v0
	v_mov_b32_e32 v20, v0
	v_mov_b32_e32 v21, v0
	v_mov_b32_e32 v22, v0
	v_mov_b32_e32 v23, v0
	v_mov_b32_e32 v32, v0
	v_mov_b32_e32 v33, v0
	v_mov_b32_e32 v34, v0
	v_mov_b32_e32 v35, v0
	v_mov_b32_e32 v36, v0
	v_mov_b32_e32 v37, v0
	v_mov_b32_e32 v38, v0
	v_mov_b32_e32 v39, v0
	v_mov_b32_e32 v48, v0
	v_mov_b32_e32 v49, v0
	v_mov_b32_e32 v50, v0
	v_mov_b32_e32 v51, v0
	v_mov_b32_e32 v52, v0
	v_mov_b32_e32 v53, v0
	v_mov_b32_e32 v54, v0
	v_mov_b32_e32 v55, v0
	v_mov_b32_e32 v56, v0
	v_mov_b32_e32 v57, v0
	v_mov_b32_e32 v58, v0
	v_mov_b32_e32 v59, v0
	v_mov_b32_e32 v60, v0
	v_mov_b32_e32 v61, v0
	v_mov_b32_e32 v62, v0
	v_mov_b32_e32 v63, v0
	v_mov_b32_e32 v64, v0
	v_mov_b32_e32 v65, v0
	v_mov_b32_e32 v66, v0
	v_mov_b32_e32 v67, v0
	v_mov_b32_e32 v68, v0
	v_mov_b32_e32 v69, v0
	v_mov_b32_e32 v70, v0
	v_mov_b32_e32 v71, v0
	v_mov_b32_e32 v72, v0
	v_mov_b32_e32 v73, v0
	v_mov_b32_e32 v74, v0
	v_mov_b32_e32 v75, v0
	v_mov_b32_e32 v76, v0
	v_mov_b32_e32 v77, v0
	v_mov_b32_e32 v78, v0
	v_mov_b32_e32 v79, v0
	v_mov_b32_e32 v88, v0
	v_mov_b32_e32 v89, v0
	v_mov_b32_e32 v90, v0
	v_mov_b32_e32 v91, v0
	v_mov_b32_e32 v92, v0
	v_mov_b32_e32 v93, v0
	v_mov_b32_e32 v94, v0
	v_mov_b32_e32 v95, v0
	v_mov_b32_e32 v104, v0
	v_mov_b32_e32 v105, v0
	v_mov_b32_e32 v106, v0
	v_mov_b32_e32 v107, v0
	v_mov_b32_e32 v108, v0
	v_mov_b32_e32 v109, v0
	v_mov_b32_e32 v110, v0
	v_mov_b32_e32 v111, v0
	v_mov_b32_e32 v80, v0
	v_mov_b32_e32 v81, v0
	v_mov_b32_e32 v82, v0
	v_mov_b32_e32 v83, v0
	v_mov_b32_e32 v84, v0
	v_mov_b32_e32 v85, v0
	v_mov_b32_e32 v86, v0
	v_mov_b32_e32 v87, v0
	v_mov_b32_e32 v96, v0
	v_mov_b32_e32 v97, v0
	v_mov_b32_e32 v98, v0
	v_mov_b32_e32 v99, v0
	v_mov_b32_e32 v100, v0
	v_mov_b32_e32 v101, v0
	v_mov_b32_e32 v102, v0
	v_mov_b32_e32 v103, v0
	v_mov_b32_e32 v112, v0
	v_mov_b32_e32 v113, v0
	v_mov_b32_e32 v114, v0
	v_mov_b32_e32 v115, v0
	v_mov_b32_e32 v116, v0
	v_mov_b32_e32 v117, v0
	v_mov_b32_e32 v118, v0
	v_mov_b32_e32 v119, v0
	v_mov_b32_e32 v120, v0
	v_mov_b32_e32 v121, v0
	v_mov_b32_e32 v122, v0
	v_mov_b32_e32 v123, v0
	v_mov_b32_e32 v124, v0
	v_mov_b32_e32 v125, v0
	v_mov_b32_e32 v126, v0
	v_mov_b32_e32 v127, v0
	.p2align	6

.LBB0_722:
	s_andn2_b64 vcc, exec, s[14:15]
	s_cbranch_vccz .LBB0_725
	.p2align	6

.LBB0_899:
	s_ashr_i32 s29, s28, 31
	s_lshl_b64 s[36:37], s[28:29], 20
	s_ashr_i32 s27, s26, 31
	v_lshl_add_u64 v[146:147], v[128:129], 0, s[36:37]
	s_lshl_b64 s[36:37], s[26:27], 20
	v_lshl_add_u64 v[150:151], v[130:131], 0, s[36:37]
	v_lshl_add_u64 v[152:153], v[156:157], 0, s[22:23]
	v_cndmask_b32_e64 v155, v145, v147, s[6:7]
	v_cndmask_b32_e64 v154, v144, v146, s[6:7]
	v_cndmask_b32_e64 v157, v157, v151, s[6:7]
	v_cndmask_b32_e64 v156, v156, v150, s[6:7]
	v_lshl_add_u64 v[158:159], v[144:145], 0, v[136:137]
	v_lshl_add_u64 v[166:167], v[144:145], 0, v[138:139]
	s_mov_b32 s27, -2
	s_mov_b64 s[36:37], 0
	.p2align	6

.LBB0_995:
	s_ashr_i32 s27, s26, 31
	s_lshl_b64 s[6:7], s[26:27], 20
	s_ashr_i32 s25, s24, 31
	v_lshl_add_u64 v[4:5], v[160:161], 0, s[6:7]
	s_lshl_b64 s[6:7], s[24:25], 20
	v_lshl_add_u64 v[6:7], v[128:129], 0, s[6:7]
	s_ashr_i32 s23, s22, 31
	v_cndmask_b32_e64 v7, v1, v7, s[4:5]
	v_cndmask_b32_e64 v6, v0, v6, s[4:5]
	s_lshl_b64 s[6:7], s[22:23], 7
	v_cndmask_b32_e64 v5, v3, v5, s[4:5]
	v_cndmask_b32_e64 v4, v2, v4, s[4:5]
	v_lshl_add_u64 v[156:157], v[6:7], 0, s[6:7]
	v_lshl_add_u64 v[154:155], v[4:5], 0, s[6:7]
	v_cndmask_b32_e64 v158, v0, v156, s[4:5]
	v_lshl_add_u64 v[170:171], v[0:1], 0, s[20:21]
	v_mov_b32_e32 v0, 0
	v_cndmask_b32_e64 v159, v3, v155, s[4:5]
	v_cndmask_b32_e64 v138, v2, v154, s[4:5]
	v_cndmask_b32_e64 v167, v1, v157, s[4:5]
	s_add_i32 s6, s40, -2
	v_lshl_add_u64 v[168:169], v[2:3], 0, s[16:17]
	s_mov_b32 s7, 0
	v_mov_b32_e32 v1, v0
	v_mov_b32_e32 v2, v0
	v_mov_b32_e32 v3, v0
	v_mov_b32_e32 v8, v0
	v_mov_b32_e32 v9, v0
	v_mov_b32_e32 v10, v0
	v_mov_b32_e32 v11, v0
	v_mov_b32_e32 v16, v0
	v_mov_b32_e32 v17, v0
	v_mov_b32_e32 v18, v0
	v_mov_b32_e32 v19, v0
	v_mov_b32_e32 v24, v0
	v_mov_b32_e32 v25, v0
	v_mov_b32_e32 v26, v0
	v_mov_b32_e32 v27, v0
	v_mov_b32_e32 v32, v0
	v_mov_b32_e32 v33, v0
	v_mov_b32_e32 v34, v0
	v_mov_b32_e32 v35, v0
	v_mov_b32_e32 v40, v0
	v_mov_b32_e32 v41, v0
	v_mov_b32_e32 v42, v0
	v_mov_b32_e32 v43, v0
	v_mov_b32_e32 v48, v0
	v_mov_b32_e32 v49, v0
	v_mov_b32_e32 v50, v0
	v_mov_b32_e32 v51, v0
	v_mov_b32_e32 v56, v0
	v_mov_b32_e32 v57, v0
	v_mov_b32_e32 v58, v0
	v_mov_b32_e32 v59, v0
	v_mov_b32_e32 v4, v0
	v_mov_b32_e32 v5, v0
	v_mov_b32_e32 v6, v0
	v_mov_b32_e32 v7, v0
	v_mov_b32_e32 v12, v0
	v_mov_b32_e32 v13, v0
	v_mov_b32_e32 v14, v0
	v_mov_b32_e32 v15, v0
	v_mov_b32_e32 v20, v0
	v_mov_b32_e32 v21, v0
	v_mov_b32_e32 v22, v0
	v_mov_b32_e32 v23, v0
	v_mov_b32_e32 v28, v0
	v_mov_b32_e32 v29, v0
	v_mov_b32_e32 v30, v0
	v_mov_b32_e32 v31, v0
	v_mov_b32_e32 v36, v0
	v_mov_b32_e32 v37, v0
	v_mov_b32_e32 v38, v0
	v_mov_b32_e32 v39, v0
	v_mov_b32_e32 v44, v0
	v_mov_b32_e32 v45, v0
	v_mov_b32_e32 v46, v0
	v_mov_b32_e32 v47, v0
	v_mov_b32_e32 v52, v0
	v_mov_b32_e32 v53, v0
	v_mov_b32_e32 v54, v0
	v_mov_b32_e32 v55, v0
	v_mov_b32_e32 v60, v0
	v_mov_b32_e32 v61, v0
	v_mov_b32_e32 v62, v0
	v_mov_b32_e32 v63, v0
	v_mov_b32_e32 v64, v0
	v_mov_b32_e32 v65, v0
	v_mov_b32_e32 v66, v0
	v_mov_b32_e32 v67, v0
	v_mov_b32_e32 v72, v0
	v_mov_b32_e32 v73, v0
	v_mov_b32_e32 v74, v0
	v_mov_b32_e32 v75, v0
	v_mov_b32_e32 v80, v0
	v_mov_b32_e32 v81, v0
	v_mov_b32_e32 v82, v0
	v_mov_b32_e32 v83, v0
	v_mov_b32_e32 v88, v0
	v_mov_b32_e32 v89, v0
	v_mov_b32_e32 v90, v0
	v_mov_b32_e32 v91, v0
	v_mov_b32_e32 v96, v0
	v_mov_b32_e32 v97, v0
	v_mov_b32_e32 v98, v0
	v_mov_b32_e32 v99, v0
	v_mov_b32_e32 v104, v0
	v_mov_b32_e32 v105, v0
	v_mov_b32_e32 v106, v0
	v_mov_b32_e32 v107, v0
	v_mov_b32_e32 v112, v0
	v_mov_b32_e32 v113, v0
	v_mov_b32_e32 v114, v0
	v_mov_b32_e32 v115, v0
	v_mov_b32_e32 v120, v0
	v_mov_b32_e32 v121, v0
	v_mov_b32_e32 v122, v0
	v_mov_b32_e32 v123, v0
	v_mov_b32_e32 v68, v0
	v_mov_b32_e32 v69, v0
	v_mov_b32_e32 v70, v0
	v_mov_b32_e32 v71, v0
	v_mov_b32_e32 v76, v0
	v_mov_b32_e32 v77, v0
	v_mov_b32_e32 v78, v0
	v_mov_b32_e32 v79, v0
	v_mov_b32_e32 v84, v0
	v_mov_b32_e32 v85, v0
	v_mov_b32_e32 v86, v0
	v_mov_b32_e32 v87, v0
	v_mov_b32_e32 v92, v0
	v_mov_b32_e32 v93, v0
	v_mov_b32_e32 v94, v0
	v_mov_b32_e32 v95, v0
	v_mov_b32_e32 v100, v0
	v_mov_b32_e32 v101, v0
	v_mov_b32_e32 v102, v0
	v_mov_b32_e32 v103, v0
	v_mov_b32_e32 v108, v0
	v_mov_b32_e32 v109, v0
	v_mov_b32_e32 v110, v0
	v_mov_b32_e32 v111, v0
	v_mov_b32_e32 v116, v0
	v_mov_b32_e32 v117, v0
	v_mov_b32_e32 v118, v0
	v_mov_b32_e32 v119, v0
	v_mov_b32_e32 v124, v0
	v_mov_b32_e32 v125, v0
	v_mov_b32_e32 v126, v0
	v_mov_b32_e32 v127, v0
	.p2align	6

.LBB0_1134:
	v_lshl_add_u64 v[150:151], v[150:151], 0, s[24:25]
	v_lshl_add_u64 v[152:153], v[142:143], 0, v[134:135]
	v_lshl_add_u64 v[154:155], v[142:143], 0, v[136:137]
	s_mov_b32 s29, -2
	s_mov_b64 s[10:11], 0
	.p2align	6

.LBB0_1230:
	s_ashr_i32 s23, s22, 31
	s_lshl_b64 s[24:25], s[22:23], 20
	s_add_u32 s0, s11, s24
	s_addc_u32 s1, s65, s25
	s_and_b64 s[24:25], s[4:5], exec
	s_cselect_b32 s1, s1, s29
	s_cselect_b32 s0, s0, s28
	s_ashr_i32 s21, s20, 31
	s_lshl_b64 s[24:25], s[20:21], 20
	s_add_u32 s19, s80, s24
	s_addc_u32 s21, s81, s25
	s_and_b64 s[24:25], s[4:5], exec
	s_cselect_b32 s21, s21, s31
	s_cselect_b32 s23, s19, s30
	s_ashr_i32 s19, s18, 31
	s_lshl_b64 s[26:27], s[18:19], 7
	s_add_u32 s24, s0, s26
	s_addc_u32 s25, s1, s27
	s_add_u32 s26, s23, s26
	s_addc_u32 s27, s21, s27
	s_and_b64 s[36:37], s[4:5], exec
	s_cselect_b32 s19, s25, s29
	s_cselect_b32 s21, s24, s28
	s_cselect_b32 s23, s27, s31
	s_cselect_b32 s39, s26, s30
	s_add_i32 s40, s38, -2
	s_add_u32 s28, s28, 0x80080
	s_addc_u32 s29, s29, 0
	s_add_u32 s41, s30, 0x100
	v_mov_b32_e32 v0, 0
	s_addc_u32 s42, s31, 0
	s_mov_b32 s30, 0
	v_mov_b32_e32 v1, v0
	v_mov_b32_e32 v2, v0
	v_mov_b32_e32 v3, v0
	v_mov_b32_e32 v4, v0
	v_mov_b32_e32 v5, v0
	v_mov_b32_e32 v6, v0
	v_mov_b32_e32 v7, v0
	v_mov_b32_e32 v8, v0
	v_mov_b32_e32 v9, v0
	v_mov_b32_e32 v10, v0
	v_mov_b32_e32 v11, v0
	v_mov_b32_e32 v16, v0
	v_mov_b32_e32 v17, v0
	v_mov_b32_e32 v18, v0
	v_mov_b32_e32 v19, v0
	v_mov_b32_e32 v24, v0
	v_mov_b32_e32 v25, v0
	v_mov_b32_e32 v26, v0
	v_mov_b32_e32 v27, v0
	v_mov_b32_e32 v32, v0
	v_mov_b32_e32 v33, v0
	v_mov_b32_e32 v34, v0
	v_mov_b32_e32 v35, v0
	v_mov_b32_e32 v40, v0
	v_mov_b32_e32 v41, v0
	v_mov_b32_e32 v42, v0
	v_mov_b32_e32 v43, v0
	v_mov_b32_e32 v48, v0
	v_mov_b32_e32 v49, v0
	v_mov_b32_e32 v50, v0
	v_mov_b32_e32 v51, v0
	v_mov_b32_e32 v12, v0
	v_mov_b32_e32 v13, v0
	v_mov_b32_e32 v14, v0
	v_mov_b32_e32 v15, v0
	v_mov_b32_e32 v20, v0
	v_mov_b32_e32 v21, v0
	v_mov_b32_e32 v22, v0
	v_mov_b32_e32 v23, v0
	v_mov_b32_e32 v28, v0
	v_mov_b32_e32 v29, v0
	v_mov_b32_e32 v30, v0
	v_mov_b32_e32 v31, v0
	v_mov_b32_e32 v36, v0
	v_mov_b32_e32 v37, v0
	v_mov_b32_e32 v38, v0
	v_mov_b32_e32 v39, v0
	v_mov_b32_e32 v44, v0
	v_mov_b32_e32 v45, v0
	v_mov_b32_e32 v46, v0
	v_mov_b32_e32 v47, v0
	v_mov_b32_e32 v52, v0
	v_mov_b32_e32 v53, v0
	v_mov_b32_e32 v54, v0
	v_mov_b32_e32 v55, v0
	v_mov_b32_e32 v56, v0
	v_mov_b32_e32 v57, v0
	v_mov_b32_e32 v58, v0
	v_mov_b32_e32 v59, v0
	v_mov_b32_e32 v60, v0
	v_mov_b32_e32 v61, v0
	v_mov_b32_e32 v62, v0
	v_mov_b32_e32 v63, v0
	v_mov_b32_e32 v64, v0
	v_mov_b32_e32 v65, v0
	v_mov_b32_e32 v66, v0
	v_mov_b32_e32 v67, v0
	v_mov_b32_e32 v68, v0
	v_mov_b32_e32 v69, v0
	v_mov_b32_e32 v70, v0
	v_mov_b32_e32 v71, v0
	v_mov_b32_e32 v72, v0
	v_mov_b32_e32 v73, v0
	v_mov_b32_e32 v74, v0
	v_mov_b32_e32 v75, v0
	v_mov_b32_e32 v80, v0
	v_mov_b32_e32 v81, v0
	v_mov_b32_e32 v82, v0
	v_mov_b32_e32 v83, v0
	v_mov_b32_e32 v88, v0
	v_mov_b32_e32 v89, v0
	v_mov_b32_e32 v90, v0
	v_mov_b32_e32 v91, v0
	v_mov_b32_e32 v96, v0
	v_mov_b32_e32 v97, v0
	v_mov_b32_e32 v98, v0
	v_mov_b32_e32 v99, v0
	v_mov_b32_e32 v104, v0
	v_mov_b32_e32 v105, v0
	v_mov_b32_e32 v106, v0
	v_mov_b32_e32 v107, v0
	v_mov_b32_e32 v112, v0
	v_mov_b32_e32 v113, v0
	v_mov_b32_e32 v114, v0
	v_mov_b32_e32 v115, v0
	v_mov_b32_e32 v76, v0
	v_mov_b32_e32 v77, v0
	v_mov_b32_e32 v78, v0
	v_mov_b32_e32 v79, v0
	v_mov_b32_e32 v84, v0
	v_mov_b32_e32 v85, v0
	v_mov_b32_e32 v86, v0
	v_mov_b32_e32 v87, v0
	v_mov_b32_e32 v92, v0
	v_mov_b32_e32 v93, v0
	v_mov_b32_e32 v94, v0
	v_mov_b32_e32 v95, v0
	v_mov_b32_e32 v100, v0
	v_mov_b32_e32 v101, v0
	v_mov_b32_e32 v102, v0
	v_mov_b32_e32 v103, v0
	v_mov_b32_e32 v108, v0
	v_mov_b32_e32 v109, v0
	v_mov_b32_e32 v110, v0
	v_mov_b32_e32 v111, v0
	v_mov_b32_e32 v116, v0
	v_mov_b32_e32 v117, v0
	v_mov_b32_e32 v118, v0
	v_mov_b32_e32 v119, v0
	v_mov_b32_e32 v120, v0
	v_mov_b32_e32 v121, v0
	v_mov_b32_e32 v122, v0
	v_mov_b32_e32 v123, v0
	v_mov_b32_e32 v124, v0
	v_mov_b32_e32 v125, v0
	v_mov_b32_e32 v126, v0
	v_mov_b32_e32 v127, v0
	.p2align	6

.LBB0_1816:
	s_andn2_b64 vcc, exec, s[4:5]
	s_cbranch_vccz .LBB0_1819
	.p2align	6

.LBB0_1993:
	s_ashr_i32 s25, s24, 31
	s_lshl_b64 s[0:1], s[24:25], 20
	s_add_u32 s28, s35, s0
	s_addc_u32 s29, s44, s1
	s_and_b64 s[0:1], s[4:5], exec
	s_cselect_b32 s25, s29, s39
	s_cselect_b32 s65, s28, s38
	s_ashr_i32 s27, s26, 31
	s_lshl_b64 s[0:1], s[26:27], 20
	s_add_u32 s30, s45, s0
	s_addc_u32 s31, s46, s1
	s_and_b64 s[0:1], s[4:5], exec
	s_cselect_b32 s27, s31, s41
	s_cselect_b32 s66, s30, s40
	s_add_u32 s38, s38, 0x80080
	s_addc_u32 s39, s39, 0
	s_add_u32 s67, s40, 0x100
	v_mov_b32_e32 v0, 0
	s_addc_u32 s68, s41, 0
	s_mov_b32 s69, -2
	v_mov_b32_e32 v1, v0
	v_mov_b32_e32 v2, v0
	v_mov_b32_e32 v3, v0
	v_mov_b32_e32 v4, v0
	v_mov_b32_e32 v5, v0
	v_mov_b32_e32 v6, v0
	v_mov_b32_e32 v7, v0
	v_mov_b32_e32 v8, v0
	v_mov_b32_e32 v9, v0
	v_mov_b32_e32 v10, v0
	v_mov_b32_e32 v11, v0
	v_mov_b32_e32 v20, v0
	v_mov_b32_e32 v21, v0
	v_mov_b32_e32 v22, v0
	v_mov_b32_e32 v23, v0
	v_mov_b32_e32 v24, v0
	v_mov_b32_e32 v25, v0
	v_mov_b32_e32 v26, v0
	v_mov_b32_e32 v27, v0
	v_mov_b32_e32 v36, v0
	v_mov_b32_e32 v37, v0
	v_mov_b32_e32 v38, v0
	v_mov_b32_e32 v39, v0
	v_mov_b32_e32 v40, v0
	v_mov_b32_e32 v41, v0
	v_mov_b32_e32 v42, v0
	v_mov_b32_e32 v43, v0
	v_mov_b32_e32 v52, v0
	v_mov_b32_e32 v53, v0
	v_mov_b32_e32 v54, v0
	v_mov_b32_e32 v55, v0
	v_mov_b32_e32 v12, v0
	v_mov_b32_e32 v13, v0
	v_mov_b32_e32 v14, v0
	v_mov_b32_e32 v15, v0
	v_mov_b32_e32 v16, v0
	v_mov_b32_e32 v17, v0
	v_mov_b32_e32 v18, v0
	v_mov_b32_e32 v19, v0
	v_mov_b32_e32 v28, v0
	v_mov_b32_e32 v29, v0
	v_mov_b32_e32 v30, v0
	v_mov_b32_e32 v31, v0
	v_mov_b32_e32 v32, v0
	v_mov_b32_e32 v33, v0
	v_mov_b32_e32 v34, v0
	v_mov_b32_e32 v35, v0
	v_mov_b32_e32 v44, v0
	v_mov_b32_e32 v45, v0
	v_mov_b32_e32 v46, v0
	v_mov_b32_e32 v47, v0
	v_mov_b32_e32 v48, v0
	v_mov_b32_e32 v49, v0
	v_mov_b32_e32 v50, v0
	v_mov_b32_e32 v51, v0
	v_mov_b32_e32 v56, v0
	v_mov_b32_e32 v57, v0
	v_mov_b32_e32 v58, v0
	v_mov_b32_e32 v59, v0
	v_mov_b32_e32 v60, v0
	v_mov_b32_e32 v61, v0
	v_mov_b32_e32 v62, v0
	v_mov_b32_e32 v63, v0
	v_mov_b32_e32 v64, v0
	v_mov_b32_e32 v65, v0
	v_mov_b32_e32 v66, v0
	v_mov_b32_e32 v67, v0
	v_mov_b32_e32 v68, v0
	v_mov_b32_e32 v69, v0
	v_mov_b32_e32 v70, v0
	v_mov_b32_e32 v71, v0
	v_mov_b32_e32 v72, v0
	v_mov_b32_e32 v73, v0
	v_mov_b32_e32 v74, v0
	v_mov_b32_e32 v75, v0
	v_mov_b32_e32 v84, v0
	v_mov_b32_e32 v85, v0
	v_mov_b32_e32 v86, v0
	v_mov_b32_e32 v87, v0
	v_mov_b32_e32 v88, v0
	v_mov_b32_e32 v89, v0
	v_mov_b32_e32 v90, v0
	v_mov_b32_e32 v91, v0
	v_mov_b32_e32 v100, v0
	v_mov_b32_e32 v101, v0
	v_mov_b32_e32 v102, v0
	v_mov_b32_e32 v103, v0
	v_mov_b32_e32 v104, v0
	v_mov_b32_e32 v105, v0
	v_mov_b32_e32 v106, v0
	v_mov_b32_e32 v107, v0
	v_mov_b32_e32 v116, v0
	v_mov_b32_e32 v117, v0
	v_mov_b32_e32 v118, v0
	v_mov_b32_e32 v119, v0
	v_mov_b32_e32 v76, v0
	v_mov_b32_e32 v77, v0
	v_mov_b32_e32 v78, v0
	v_mov_b32_e32 v79, v0
	v_mov_b32_e32 v80, v0
	v_mov_b32_e32 v81, v0
	v_mov_b32_e32 v82, v0
	v_mov_b32_e32 v83, v0
	v_mov_b32_e32 v92, v0
	v_mov_b32_e32 v93, v0
	v_mov_b32_e32 v94, v0
	v_mov_b32_e32 v95, v0
	v_mov_b32_e32 v96, v0
	v_mov_b32_e32 v97, v0
	v_mov_b32_e32 v98, v0
	v_mov_b32_e32 v99, v0
	v_mov_b32_e32 v108, v0
	v_mov_b32_e32 v109, v0
	v_mov_b32_e32 v110, v0
	v_mov_b32_e32 v111, v0
	v_mov_b32_e32 v112, v0
	v_mov_b32_e32 v113, v0
	v_mov_b32_e32 v114, v0
	v_mov_b32_e32 v115, v0
	v_mov_b32_e32 v120, v0
	v_mov_b32_e32 v121, v0
	v_mov_b32_e32 v122, v0
	v_mov_b32_e32 v123, v0
	v_mov_b32_e32 v124, v0
	v_mov_b32_e32 v125, v0
	v_mov_b32_e32 v126, v0
	v_mov_b32_e32 v127, v0
	.p2align	6

.LBB0_2153:
	s_ashr_i32 s19, s18, 31
	s_lshl_b64 s[0:1], s[18:19], 19
	s_add_u32 s4, s11, s0
	s_addc_u32 s5, s13, s1
	s_and_b64 s[0:1], s[20:21], exec
	s_cselect_b32 s5, s5, s27
	s_cselect_b32 s4, s4, s26
	s_ashr_i32 s17, s16, 31
	s_lshl_b64 s[0:1], s[16:17], 19
	s_add_u32 s15, s66, s0
	s_addc_u32 s17, s67, s1
	s_and_b64 s[0:1], s[20:21], exec
	s_cselect_b32 s17, s17, s29
	s_cselect_b32 s19, s15, s28
	s_ashr_i32 s15, s14, 31
	s_lshl_b64 s[0:1], s[14:15], 7
	s_add_u32 s4, s4, s0
	s_addc_u32 s5, s5, s1
	s_add_u32 s22, s19, s0
	s_addc_u32 s23, s17, s1
	s_and_b64 s[0:1], s[20:21], exec
	s_cselect_b32 s15, s23, s29
	s_cselect_b32 s17, s22, s28
	s_cselect_b32 s19, s5, s27
	s_cselect_b32 s36, s4, s26
	s_add_i32 s37, s33, -2
	s_add_u32 s26, s26, 0x40080
	s_addc_u32 s27, s27, 0
	s_add_u32 s38, s28, 0x100
	v_mov_b32_e32 v32, 0
	s_addc_u32 s39, s29, 0
	s_mov_b32 s28, 0
	v_mov_b32_e32 v33, v32
	v_mov_b32_e32 v34, v32
	v_mov_b32_e32 v35, v32
	v_mov_b32_e32 v36, v32
	v_mov_b32_e32 v37, v32
	v_mov_b32_e32 v38, v32
	v_mov_b32_e32 v39, v32
	v_mov_b32_e32 v48, v32
	v_mov_b32_e32 v49, v32
	v_mov_b32_e32 v50, v32
	v_mov_b32_e32 v51, v32
	v_mov_b32_e32 v52, v32
	v_mov_b32_e32 v53, v32
	v_mov_b32_e32 v54, v32
	v_mov_b32_e32 v55, v32
	v_mov_b32_e32 v64, v32
	v_mov_b32_e32 v65, v32
	v_mov_b32_e32 v66, v32
	v_mov_b32_e32 v67, v32
	v_mov_b32_e32 v68, v32
	v_mov_b32_e32 v69, v32
	v_mov_b32_e32 v70, v32
	v_mov_b32_e32 v71, v32
	v_mov_b32_e32 v80, v32
	v_mov_b32_e32 v81, v32
	v_mov_b32_e32 v82, v32
	v_mov_b32_e32 v83, v32
	v_mov_b32_e32 v84, v32
	v_mov_b32_e32 v85, v32
	v_mov_b32_e32 v86, v32
	v_mov_b32_e32 v87, v32
	v_mov_b32_e32 v40, v32
	v_mov_b32_e32 v41, v32
	v_mov_b32_e32 v42, v32
	v_mov_b32_e32 v43, v32
	v_mov_b32_e32 v44, v32
	v_mov_b32_e32 v45, v32
	v_mov_b32_e32 v46, v32
	v_mov_b32_e32 v47, v32
	v_mov_b32_e32 v56, v32
	v_mov_b32_e32 v57, v32
	v_mov_b32_e32 v58, v32
	v_mov_b32_e32 v59, v32
	v_mov_b32_e32 v60, v32
	v_mov_b32_e32 v61, v32
	v_mov_b32_e32 v62, v32
	v_mov_b32_e32 v63, v32
	v_mov_b32_e32 v72, v32
	v_mov_b32_e32 v73, v32
	v_mov_b32_e32 v74, v32
	v_mov_b32_e32 v75, v32
	v_mov_b32_e32 v76, v32
	v_mov_b32_e32 v77, v32
	v_mov_b32_e32 v78, v32
	v_mov_b32_e32 v79, v32
	v_mov_b32_e32 v88, v32
	v_mov_b32_e32 v89, v32
	v_mov_b32_e32 v90, v32
	v_mov_b32_e32 v91, v32
	v_mov_b32_e32 v92, v32
	v_mov_b32_e32 v93, v32
	v_mov_b32_e32 v94, v32
	v_mov_b32_e32 v95, v32
	v_mov_b32_e32 v96, v32
	v_mov_b32_e32 v97, v32
	v_mov_b32_e32 v98, v32
	v_mov_b32_e32 v99, v32
	v_mov_b32_e32 v100, v32
	v_mov_b32_e32 v101, v32
	v_mov_b32_e32 v102, v32
	v_mov_b32_e32 v103, v32
	v_mov_b32_e32 v112, v32
	v_mov_b32_e32 v113, v32
	v_mov_b32_e32 v114, v32
	v_mov_b32_e32 v115, v32
	v_mov_b32_e32 v116, v32
	v_mov_b32_e32 v117, v32
	v_mov_b32_e32 v118, v32
	v_mov_b32_e32 v119, v32
	v_mov_b32_e32 v128, v32
	v_mov_b32_e32 v129, v32
	v_mov_b32_e32 v130, v32
	v_mov_b32_e32 v131, v32
	v_mov_b32_e32 v132, v32
	v_mov_b32_e32 v133, v32
	v_mov_b32_e32 v134, v32
	v_mov_b32_e32 v135, v32
	v_mov_b32_e32 v144, v32
	v_mov_b32_e32 v145, v32
	v_mov_b32_e32 v146, v32
	v_mov_b32_e32 v147, v32
	v_mov_b32_e32 v148, v32
	v_mov_b32_e32 v149, v32
	v_mov_b32_e32 v150, v32
	v_mov_b32_e32 v151, v32
	v_mov_b32_e32 v104, v32
	v_mov_b32_e32 v105, v32
	v_mov_b32_e32 v106, v32
	v_mov_b32_e32 v107, v32
	v_mov_b32_e32 v108, v32
	v_mov_b32_e32 v109, v32
	v_mov_b32_e32 v110, v32
	v_mov_b32_e32 v111, v32
	v_mov_b32_e32 v120, v32
	v_mov_b32_e32 v121, v32
	v_mov_b32_e32 v122, v32
	v_mov_b32_e32 v123, v32
	v_mov_b32_e32 v124, v32
	v_mov_b32_e32 v125, v32
	v_mov_b32_e32 v126, v32
	v_mov_b32_e32 v127, v32
	v_mov_b32_e32 v136, v32
	v_mov_b32_e32 v137, v32
	v_mov_b32_e32 v138, v32
	v_mov_b32_e32 v139, v32
	v_mov_b32_e32 v140, v32
	v_mov_b32_e32 v141, v32
	v_mov_b32_e32 v142, v32
	v_mov_b32_e32 v143, v32
	v_mov_b32_e32 v152, v32
	v_mov_b32_e32 v153, v32
	v_mov_b32_e32 v154, v32
	v_mov_b32_e32 v155, v32
	v_mov_b32_e32 v156, v32
	v_mov_b32_e32 v157, v32
	v_mov_b32_e32 v158, v32
	v_mov_b32_e32 v159, v32
	.p2align	6

.LBB0_2315:
	s_ashr_i32 s17, s16, 31
	s_lshl_b64 s[0:1], s[16:17], 7
	s_and_b64 s[26:27], s[26:27], exec
	s_cselect_b32 s0, s0, 0
	s_cselect_b32 s1, s1, 0
	s_add_u32 s18, s18, s0
	s_addc_u32 s19, s19, s1
	s_add_u32 s20, s20, s0
	s_addc_u32 s21, s21, s1
	s_add_i32 s17, s30, -2
	s_add_u32 s31, s24, 0x100
	v_mov_b32_e32 v32, 0
	s_mov_b32 s28, 0
	s_addc_u32 s33, s25, 0
	v_mov_b32_e32 v33, v32
	v_mov_b32_e32 v34, v32
	v_mov_b32_e32 v35, v32
	v_mov_b32_e32 v36, v32
	v_mov_b32_e32 v37, v32
	v_mov_b32_e32 v38, v32
	v_mov_b32_e32 v39, v32
	v_mov_b32_e32 v48, v32
	v_mov_b32_e32 v49, v32
	v_mov_b32_e32 v50, v32
	v_mov_b32_e32 v51, v32
	v_mov_b32_e32 v52, v32
	v_mov_b32_e32 v53, v32
	v_mov_b32_e32 v54, v32
	v_mov_b32_e32 v55, v32
	v_mov_b32_e32 v64, v32
	v_mov_b32_e32 v65, v32
	v_mov_b32_e32 v66, v32
	v_mov_b32_e32 v67, v32
	v_mov_b32_e32 v68, v32
	v_mov_b32_e32 v69, v32
	v_mov_b32_e32 v70, v32
	v_mov_b32_e32 v71, v32
	v_mov_b32_e32 v80, v32
	v_mov_b32_e32 v81, v32
	v_mov_b32_e32 v82, v32
	v_mov_b32_e32 v83, v32
	v_mov_b32_e32 v84, v32
	v_mov_b32_e32 v85, v32
	v_mov_b32_e32 v86, v32
	v_mov_b32_e32 v87, v32
	v_mov_b32_e32 v40, v32
	v_mov_b32_e32 v41, v32
	v_mov_b32_e32 v42, v32
	v_mov_b32_e32 v43, v32
	v_mov_b32_e32 v44, v32
	v_mov_b32_e32 v45, v32
	v_mov_b32_e32 v46, v32
	v_mov_b32_e32 v47, v32
	v_mov_b32_e32 v56, v32
	v_mov_b32_e32 v57, v32
	v_mov_b32_e32 v58, v32
	v_mov_b32_e32 v59, v32
	v_mov_b32_e32 v60, v32
	v_mov_b32_e32 v61, v32
	v_mov_b32_e32 v62, v32
	v_mov_b32_e32 v63, v32
	v_mov_b32_e32 v72, v32
	v_mov_b32_e32 v73, v32
	v_mov_b32_e32 v74, v32
	v_mov_b32_e32 v75, v32
	v_mov_b32_e32 v76, v32
	v_mov_b32_e32 v77, v32
	v_mov_b32_e32 v78, v32
	v_mov_b32_e32 v79, v32
	v_mov_b32_e32 v88, v32
	v_mov_b32_e32 v89, v32
	v_mov_b32_e32 v90, v32
	v_mov_b32_e32 v91, v32
	v_mov_b32_e32 v92, v32
	v_mov_b32_e32 v93, v32
	v_mov_b32_e32 v94, v32
	v_mov_b32_e32 v95, v32
	v_mov_b32_e32 v96, v32
	v_mov_b32_e32 v97, v32
	v_mov_b32_e32 v98, v32
	v_mov_b32_e32 v99, v32
	v_mov_b32_e32 v100, v32
	v_mov_b32_e32 v101, v32
	v_mov_b32_e32 v102, v32
	v_mov_b32_e32 v103, v32
	v_mov_b32_e32 v112, v32
	v_mov_b32_e32 v113, v32
	v_mov_b32_e32 v114, v32
	v_mov_b32_e32 v115, v32
	v_mov_b32_e32 v116, v32
	v_mov_b32_e32 v117, v32
	v_mov_b32_e32 v118, v32
	v_mov_b32_e32 v119, v32
	v_mov_b32_e32 v128, v32
	v_mov_b32_e32 v129, v32
	v_mov_b32_e32 v130, v32
	v_mov_b32_e32 v131, v32
	v_mov_b32_e32 v132, v32
	v_mov_b32_e32 v133, v32
	v_mov_b32_e32 v134, v32
	v_mov_b32_e32 v135, v32
	v_mov_b32_e32 v144, v32
	v_mov_b32_e32 v145, v32
	v_mov_b32_e32 v146, v32
	v_mov_b32_e32 v147, v32
	v_mov_b32_e32 v148, v32
	v_mov_b32_e32 v149, v32
	v_mov_b32_e32 v150, v32
	v_mov_b32_e32 v151, v32
	v_mov_b32_e32 v104, v32
	v_mov_b32_e32 v105, v32
	v_mov_b32_e32 v106, v32
	v_mov_b32_e32 v107, v32
	v_mov_b32_e32 v108, v32
	v_mov_b32_e32 v109, v32
	v_mov_b32_e32 v110, v32
	v_mov_b32_e32 v111, v32
	v_mov_b32_e32 v120, v32
	v_mov_b32_e32 v121, v32
	v_mov_b32_e32 v122, v32
	v_mov_b32_e32 v123, v32
	v_mov_b32_e32 v124, v32
	v_mov_b32_e32 v125, v32
	v_mov_b32_e32 v126, v32
	v_mov_b32_e32 v127, v32
	v_mov_b32_e32 v136, v32
	v_mov_b32_e32 v137, v32
	v_mov_b32_e32 v138, v32
	v_mov_b32_e32 v139, v32
	v_mov_b32_e32 v140, v32
	v_mov_b32_e32 v141, v32
	v_mov_b32_e32 v142, v32
	v_mov_b32_e32 v143, v32
	v_mov_b32_e32 v152, v32
	v_mov_b32_e32 v153, v32
	v_mov_b32_e32 v154, v32
	v_mov_b32_e32 v155, v32
	v_mov_b32_e32 v156, v32
	v_mov_b32_e32 v157, v32
	v_mov_b32_e32 v158, v32
	v_mov_b32_e32 v159, v32
	.p2align	6
